# speedup vs baseline: 1.0044x; 1.0044x over previous
	.amdhsa_kernel _Z12scan2_kernelPKDF16_S0_S0_S0_S0_PKfS2_S2_S2_PDF16_PfS4_
		.amdhsa_group_segment_fixed_size 0
		.amdhsa_private_segment_fixed_size 0
		.amdhsa_kernarg_size 96
		.amdhsa_user_sgpr_count 2
		.amdhsa_user_sgpr_dispatch_ptr 0
		.amdhsa_user_sgpr_queue_ptr 0
		.amdhsa_user_sgpr_kernarg_segment_ptr 1
		.amdhsa_user_sgpr_dispatch_id 0
		.amdhsa_user_sgpr_kernarg_preload_length 0
		.amdhsa_user_sgpr_kernarg_preload_offset 0
		.amdhsa_user_sgpr_private_segment_size 0
		.amdhsa_uses_dynamic_stack 0
		.amdhsa_enable_private_segment 0
		.amdhsa_system_sgpr_workgroup_id_x 1
		.amdhsa_system_sgpr_workgroup_id_y 0
		.amdhsa_system_sgpr_workgroup_id_z 0
		.amdhsa_system_sgpr_workgroup_info 0
		.amdhsa_system_vgpr_workitem_id 0
		.amdhsa_next_free_vgpr 252
		.amdhsa_next_free_sgpr 80
		.amdhsa_accum_offset 252
		.amdhsa_reserve_vcc 1
		.amdhsa_float_round_mode_32 0
		.amdhsa_float_round_mode_16_64 0
		.amdhsa_float_denorm_mode_32 3
		.amdhsa_float_denorm_mode_16_64 3
		.amdhsa_dx10_clamp 1
		.amdhsa_ieee_mode 1
		.amdhsa_fp16_overflow 0
		.amdhsa_tg_split 0
		.amdhsa_exception_fp_ieee_invalid_op 0
		.amdhsa_exception_fp_denorm_src 0
		.amdhsa_exception_fp_ieee_div_zero 0
		.amdhsa_exception_fp_ieee_overflow 0
		.amdhsa_exception_fp_ieee_underflow 0
		.amdhsa_exception_fp_ieee_inexact 0
		.amdhsa_exception_int_div_zero 0
	.end_amdhsa_kernel

amdhsa.kernels:
  - .agpr_count:     0
    .args:
      - .actual_access:  read_only
        .address_space:  global
        .offset:         0
        .size:           8
        .value_kind:     global_buffer
      - .actual_access:  read_only
        .address_space:  global
        .offset:         8
        .size:           8
        .value_kind:     global_buffer
      - .actual_access:  read_only
        .address_space:  global
        .offset:         16
        .size:           8
        .value_kind:     global_buffer
      - .actual_access:  read_only
        .address_space:  global
        .offset:         24
        .size:           8
        .value_kind:     global_buffer
      - .actual_access:  write_only
        .address_space:  global
        .offset:         32
        .size:           8
        .value_kind:     global_buffer
      - .actual_access:  write_only
        .address_space:  global
        .offset:         40
        .size:           8
        .value_kind:     global_buffer
      - .actual_access:  write_only
        .address_space:  global
        .offset:         48
        .size:           8
        .value_kind:     global_buffer
      - .actual_access:  write_only
        .address_space:  global
        .offset:         56
        .size:           8
        .value_kind:     global_buffer
    .group_segment_fixed_size: 16640
    .kernarg_segment_align: 8
    .kernarg_segment_size: 64
    .language:       OpenCL C
    .language_version:
      - 2
      - 0
    .max_flat_workgroup_size: 256
    .name:           _Z11prep_kernelPKfS0_S0_S0_PDF16_S1_S1_Pf
    .private_segment_fixed_size: 0
    .sgpr_count:     18
    .sgpr_spill_count: 0
    .symbol:         _Z11prep_kernelPKfS0_S0_S0_PDF16_S1_S1_Pf.kd
    .uniform_work_group_size: 1
    .uses_dynamic_stack: false
    .vgpr_count:     42
    .vgpr_spill_count: 0
    .wavefront_size: 64
  - .agpr_count:     0
    .args:
      - .address_space:  global
        .offset:         0
        .size:           8
        .value_kind:     global_buffer
      - .address_space:  global
        .offset:         8
        .size:           8
        .value_kind:     global_buffer
      - .actual_access:  write_only
        .address_space:  global
        .offset:         16
        .size:           8
        .value_kind:     global_buffer
      - .actual_access:  read_only
        .address_space:  global
        .offset:         24
        .size:           8
        .value_kind:     global_buffer
    .group_segment_fixed_size: 49152
    .kernarg_segment_align: 8
    .kernarg_segment_size: 32
    .language:       OpenCL C
    .language_version:
      - 2
      - 0
    .max_flat_workgroup_size: 512
    .name:           _Z13gemm2b_kernelPKDF16_S0_PfPKf
    .private_segment_fixed_size: 0
    .sgpr_count:     24
    .sgpr_spill_count: 0
    .symbol:         _Z13gemm2b_kernelPKDF16_S0_PfPKf.kd
    .uniform_work_group_size: 1
    .uses_dynamic_stack: false
    .vgpr_count:     176
    .vgpr_spill_count: 0
    .wavefront_size: 64
  - .agpr_count:     0
    .args:
      - .address_space:  global
        .offset:         0
        .size:           8
        .value_kind:     global_buffer
      - .address_space:  global
        .offset:         8
        .size:           8
        .value_kind:     global_buffer
      - .actual_access:  write_only
        .address_space:  global
        .offset:         16
        .size:           8
        .value_kind:     global_buffer
      - .actual_access:  write_only
        .address_space:  global
        .offset:         24
        .size:           8
        .value_kind:     global_buffer
    .group_segment_fixed_size: 16384
    .kernarg_segment_align: 8
    .kernarg_segment_size: 32
    .language:       OpenCL C
    .language_version:
      - 2
      - 0
    .max_flat_workgroup_size: 512
    .name:           _Z12gemm8_kernelPKDF16_S0_PDF16_S1_
    .private_segment_fixed_size: 0
    .sgpr_count:     58
    .sgpr_spill_count: 0
    .symbol:         _Z12gemm8_kernelPKDF16_S0_PDF16_S1_.kd
    .uniform_work_group_size: 1
    .uses_dynamic_stack: false
    .vgpr_count:     184
    .vgpr_spill_count: 0
    .wavefront_size: 64
  - .agpr_count:     0
    .args:
      - .actual_access:  read_only
        .address_space:  global
        .offset:         0
        .size:           8
        .value_kind:     global_buffer
      - .actual_access:  read_only
        .address_space:  global
        .offset:         8
        .size:           8
        .value_kind:     global_buffer
      - .actual_access:  read_only
        .address_space:  global
        .offset:         16
        .size:           8
        .value_kind:     global_buffer
      - .actual_access:  read_only
        .address_space:  global
        .offset:         24
        .size:           8
        .value_kind:     global_buffer
      - .actual_access:  write_only
        .address_space:  global
        .offset:         32
        .size:           8
        .value_kind:     global_buffer
      - .actual_access:  write_only
        .address_space:  global
        .offset:         40
        .size:           8
        .value_kind:     global_buffer
      - .actual_access:  read_only
        .address_space:  global
        .offset:         48
        .size:           8
        .value_kind:     global_buffer
      - .actual_access:  read_only
        .address_space:  global
        .offset:         56
        .size:           8
        .value_kind:     global_buffer
      - .actual_access:  read_only
        .address_space:  global
        .offset:         64
        .size:           8
        .value_kind:     global_buffer
      - .actual_access:  write_only
        .address_space:  global
        .offset:         72
        .size:           8
        .value_kind:     global_buffer
      - .actual_access:  write_only
        .address_space:  global
        .offset:         80
        .size:           8
        .value_kind:     global_buffer
      - .actual_access:  write_only
        .address_space:  global
        .offset:         88
        .size:           8
        .value_kind:     global_buffer
      - .actual_access:  write_only
        .address_space:  global
        .offset:         96
        .size:           8
        .value_kind:     global_buffer
    .group_segment_fixed_size: 17952
    .kernarg_segment_align: 8
    .kernarg_segment_size: 104
    .language:       OpenCL C
    .language_version:
      - 2
      - 0
    .max_flat_workgroup_size: 256
    .name:           _Z13convdt_kernelPKDF16_S0_PKfS2_PDF16_S3_S2_S2_S2_PfS4_S4_S4_
    .private_segment_fixed_size: 0
    .sgpr_count:     26
    .sgpr_spill_count: 0
    .symbol:         _Z13convdt_kernelPKDF16_S0_PKfS2_PDF16_S3_S2_S2_S2_PfS4_S4_S4_.kd
    .uniform_work_group_size: 1
    .uses_dynamic_stack: false
    .vgpr_count:     88
    .vgpr_spill_count: 0
    .wavefront_size: 64
  - .agpr_count:     0
    .args:
      - .actual_access:  read_only
        .address_space:  global
        .offset:         0
        .size:           8
        .value_kind:     global_buffer
      - .actual_access:  read_only
        .address_space:  global
        .offset:         8
        .size:           8
        .value_kind:     global_buffer
      - .actual_access:  read_only
        .address_space:  global
        .offset:         16
        .size:           8
        .value_kind:     global_buffer
      - .actual_access:  write_only
        .address_space:  global
        .offset:         24
        .size:           8
        .value_kind:     global_buffer
    .group_segment_fixed_size: 34816
    .kernarg_segment_align: 8
    .kernarg_segment_size: 32
    .language:       OpenCL C
    .language_version:
      - 2
      - 0
    .max_flat_workgroup_size: 256
    .name:           _Z11sloc_kernelPKDF16_PKfS2_PDF16_
    .private_segment_fixed_size: 0
    .sgpr_count:     28
    .sgpr_spill_count: 0
    .symbol:         _Z11sloc_kernelPKDF16_PKfS2_PDF16_.kd
    .uniform_work_group_size: 1
    .uses_dynamic_stack: false
    .vgpr_count:     120
    .vgpr_spill_count: 0
    .wavefront_size: 64
  - .agpr_count:     64
    .args:
      - .actual_access:  read_only
        .address_space:  global
        .offset:         0
        .size:           8
        .value_kind:     global_buffer
      - .address_space:  global
        .offset:         8
        .size:           8
        .value_kind:     global_buffer
      - .actual_access:  read_only
        .address_space:  global
        .offset:         16
        .size:           8
        .value_kind:     global_buffer
      - .actual_access:  write_only
        .address_space:  global
        .offset:         24
        .size:           8
        .value_kind:     global_buffer
    .group_segment_fixed_size: 0
    .kernarg_segment_align: 8
    .kernarg_segment_size: 32
    .language:       OpenCL C
    .language_version:
      - 2
      - 0
    .max_flat_workgroup_size: 256
    .name:           _Z12spass_kernelPKfPDF16_PKDF16_S1_
    .private_segment_fixed_size: 0
    .sgpr_count:     21
    .sgpr_spill_count: 0
    .symbol:         _Z12spass_kernelPKfPDF16_PKDF16_S1_.kd
    .uniform_work_group_size: 1
    .uses_dynamic_stack: false
    .vgpr_count:     180
    .vgpr_spill_count: 0
    .wavefront_size: 64
  - .agpr_count:     0
    .args:
      - .actual_access:  read_only
        .address_space:  global
        .offset:         0
        .size:           8
        .value_kind:     global_buffer
      - .actual_access:  read_only
        .address_space:  global
        .offset:         8
        .size:           8
        .value_kind:     global_buffer
      - .actual_access:  read_only
        .address_space:  global
        .offset:         16
        .size:           8
        .value_kind:     global_buffer
      - .actual_access:  read_only
        .address_space:  global
        .offset:         24
        .size:           8
        .value_kind:     global_buffer
      - .actual_access:  read_only
        .address_space:  global
        .offset:         32
        .size:           8
        .value_kind:     global_buffer
      - .actual_access:  read_only
        .address_space:  global
        .offset:         40
        .size:           8
        .value_kind:     global_buffer
      - .actual_access:  read_only
        .address_space:  global
        .offset:         48
        .size:           8
        .value_kind:     global_buffer
      - .actual_access:  read_only
        .address_space:  global
        .offset:         56
        .size:           8
        .value_kind:     global_buffer
      - .actual_access:  read_only
        .address_space:  global
        .offset:         64
        .size:           8
        .value_kind:     global_buffer
      - .actual_access:  write_only
        .address_space:  global
        .offset:         72
        .size:           8
        .value_kind:     global_buffer
      - .address_space:  global
        .offset:         80
        .size:           8
        .value_kind:     global_buffer
      - .actual_access:  read_only
        .address_space:  global
        .offset:         88
        .size:           8
        .value_kind:     global_buffer
    .group_segment_fixed_size: 54272
    .kernarg_segment_align: 8
    .kernarg_segment_size: 96
    .language:       OpenCL C
    .language_version:
      - 2
      - 0
    .max_flat_workgroup_size: 256
    .name:           _Z11scan_kernelPKDF16_S0_S0_S0_S0_PKfS2_S2_S2_PDF16_PfS4_
    .private_segment_fixed_size: 0
    .sgpr_count:     106
    .sgpr_spill_count: 56
    .symbol:         _Z11scan_kernelPKDF16_S0_S0_S0_S0_PKfS2_S2_S2_PDF16_PfS4_.kd
    .uniform_work_group_size: 1
    .uses_dynamic_stack: false
    .vgpr_count:     243
    .vgpr_spill_count: 0
    .wavefront_size: 64
  - .agpr_count:     0
    .args:
      - .actual_access:  read_only
        .address_space:  global
        .offset:         0
        .size:           8
        .value_kind:     global_buffer
      - .address_space:  global
        .offset:         8
        .size:           8
        .value_kind:     global_buffer
      - .address_space:  global
        .offset:         16
        .size:           8
        .value_kind:     global_buffer
      - .actual_access:  read_only
        .address_space:  global
        .offset:         24
        .size:           8
        .value_kind:     global_buffer
      - .address_space:  global
        .offset:         32
        .size:           8
        .value_kind:     global_buffer
      - .address_space:  global
        .offset:         40
        .size:           8
        .value_kind:     global_buffer
      - .address_space:  global
        .offset:         48
        .size:           8
        .value_kind:     global_buffer
      - .actual_access:  read_only
        .address_space:  global
        .offset:         56
        .size:           8
        .value_kind:     global_buffer
      - .actual_access:  read_only
        .address_space:  global
        .offset:         64
        .size:           8
        .value_kind:     global_buffer
      - .actual_access:  write_only
        .address_space:  global
        .offset:         72
        .size:           8
        .value_kind:     global_buffer
      - .address_space:  global
        .offset:         80
        .size:           8
        .value_kind:     global_buffer
      - .actual_access:  read_only
        .address_space:  global
        .offset:         88
        .size:           8
        .value_kind:     global_buffer
    .group_segment_fixed_size: 0
    .kernarg_segment_align: 8
    .kernarg_segment_size: 96
    .language:       OpenCL C
    .language_version:
      - 2
      - 0
    .max_flat_workgroup_size: 512
    .name:           _Z12scan2_kernelPKDF16_S0_S0_S0_S0_PKfS2_S2_S2_PDF16_PfS4_
    .private_segment_fixed_size: 0
    .sgpr_count:     86
    .sgpr_spill_count: 0
    .symbol:         _Z12scan2_kernelPKDF16_S0_S0_S0_S0_PKfS2_S2_S2_PDF16_PfS4_.kd
    .uniform_work_group_size: 1
    .uses_dynamic_stack: false
    .vgpr_count:     252
    .vgpr_spill_count: 0
    .wavefront_size: 64
  - .agpr_count:     64
    .args:
      - .address_space:  global
        .offset:         0
        .size:           8
        .value_kind:     global_buffer
      - .address_space:  global
        .offset:         8
        .size:           8
        .value_kind:     global_buffer
      - .offset:         16
        .size:           4
        .value_kind:     by_value
      - .offset:         20
        .size:           4
        .value_kind:     by_value
      - .offset:         24
        .size:           4
        .value_kind:     by_value
      - .actual_access:  write_only
        .address_space:  global
        .offset:         32
        .size:           8
        .value_kind:     global_buffer
      - .actual_access:  write_only
        .address_space:  global
        .offset:         40
        .size:           8
        .value_kind:     global_buffer
      - .actual_access:  read_only
        .address_space:  global
        .offset:         48
        .size:           8
        .value_kind:     global_buffer
      - .offset:         56
        .size:           4
        .value_kind:     by_value
    .group_segment_fixed_size: 131072
    .kernarg_segment_align: 8
    .kernarg_segment_size: 60
    .language:       OpenCL C
    .language_version:
      - 2
      - 0
    .max_flat_workgroup_size: 256
    .name:           _Z11gemm_kernelILi1EEvPKDF16_S1_iiiPDF16_PfPKfi
    .private_segment_fixed_size: 0
    .sgpr_count:     27
    .sgpr_spill_count: 0
    .symbol:         _Z11gemm_kernelILi1EEvPKDF16_S1_iiiPDF16_PfPKfi.kd
    .uniform_work_group_size: 1
    .uses_dynamic_stack: false
    .vgpr_count:     208
    .vgpr_spill_count: 0
    .wavefront_size: 64
